# plus GEMM prologue: second K-tile DMA issued before first wait; moe_tables recomputation skipped in MoE-down and combine (tables persist in LDS)
# speedup vs baseline: 1.0070x; 1.0070x over previous
; template <class P, class MK = NoChain>
; __device__ __forceinline__ void gemm_phase(LAS unsigned char* lds, const P& p, const MK& mk = MK(), bool chain_out = false, bool chained_in = false) {
;     ...
;     int tid = threadIdx.x; asm volatile("" : "+v"(tid));
;     const int wid = __builtin_amdgcn_readfirstlane(tid >> 6), lane = tid & 63, wr = wid >> 2, wc = wid & 3, fr = lane & 15, fq = lane >> 4;
;     unsigned voffB[2], vA[2][2], nvA[2][2], nvB[2]; typedef decltype(mk()) NP; constexpr int NES = NP::FP8 ? 1 : 2; constexpr int NBMODE = bmode_of<NP>::value; constexpr size_t nhstepB = (size_t)(NBMODE == 1 ? 8 : (NBMODE == 2 ? 16 : HALF)) * NP::LDB * NES;
;     constexpr size_t kstep = (size_t)(BK * 2);
;     constexpr int BMODE = bmode_of<P>::value;
;     constexpr size_t hstep = (size_t)(BMODE == 1 ? 8 : (BMODE == 2 ? 16 : HALF)) * LDB * ES, hstepA = (size_t)HALF * LDA * ES;
; #pragma unroll
;     for (int i = 0; i < 2; ++i) { int R, C; stage_rc(tid * 16 + i * 8192, R, C); const int rho_ = R & 31;
;         const int fq_ = (rho_ & 15) >> 2, n_ = rho_ >> 4, q_ = rho_ & 3;
;         const int Rb = BMODE == 1 ? ((R >> 5) * 64 + fq_ * 16 + 4 * n_ + q_) : (BMODE == 2 ? ((R >> 5) * 64 + 32 * (fq_ >> 1) + 8 * n_ + 4 * (fq_ & 1) + q_) : (P::PERM ? ((R & ~31) + perm32(R & 31)) : R));
;         voffB[i] = (unsigned)(Rb * LDB * ES + C * 2); vA[0][i] = (unsigned)(R * LDA * ES + C * 2); vA[1][i] = vA[0][i] + (unsigned)hstepA; nvA[0][i] = vA[0][i]; nvA[1][i] = vA[1][i]; nvB[i] = voffB[i]; }
;     const unsigned ldsw = (unsigned)wid * 1024u;
;     const int aoff = lds_byte(wr * 64 + fr, fq * 8), boff = lds_byte(wc * 32 + fr, fq * 8); const int aoff1 = aoff ^ 64, boff1 = boff ^ 64;
;     ...
;     Unit cur, nxt; int ui = 0;
;     if (!p.next(0, cur)) return;
;     Acc acc;
;     if constexpr (!PEEL) {
; #pragma unroll
;     for (int a = 0; a < 2; ++a)
; #pragma unroll
;         for (int b = 0; b < 2; ++b)
; #pragma unroll
;             for (int m = 0; m < 4; ++m)
; #pragma unroll
;                 for (int n = 0; n < 2; ++n) { typedef double d2_ __attribute__((ext_vector_type(2))); d2_ z_; asm volatile("v_mov_b64 %0, 0" : "=v"(z_.x)); asm volatile("v_mov_b64 %0, 0" : "=v"(z_.y)); acc[a][b][m][n] = __builtin_bit_cast(f32x4, z_); }
;     }
;     typedef int v8i_ __attribute__((ext_vector_type(8))); typedef int v4i_ __attribute__((ext_vector_type(4)));
.LBB0_538:
	s_add_u32 s8, s2, 0x3e400000
	s_addc_u32 s9, s3, 0
	s_lshl_b32 s1, s10, 5
	s_and_b32 s1, s1, 0x60
	s_add_u32 s10, s20, 0x80
	s_addc_u32 s11, s21, 0
	s_add_i32 s42, s36, 0x18000
	s_mov_b32 m0, s42
	v_lshl_add_u64 v[6:7], s[10:11], 0, v[194:195]
	s_add_i32 s43, s36, 0x1a000
	global_load_lds_dwordx4 v[6:7], off
	v_lshl_add_u64 v[6:7], s[10:11], 0, v[196:197]
	s_add_u32 s10, s2, 0x30c00080
	s_mov_b32 m0, s43
	s_addc_u32 s11, s3, 0
	s_add_i32 s44, s36, 0x8000
	global_load_lds_dwordx4 v[6:7], off
	s_mov_b32 m0, s44
	v_lshl_add_u64 v[6:7], s[10:11], 0, v[198:199]
	s_add_i32 s45, s36, 0xa000
	global_load_lds_dwordx4 v[6:7], off
	v_lshl_add_u64 v[6:7], s[10:11], 0, v[208:209]
	s_add_u32 s10, s20, 0x40080
	s_mov_b32 m0, s45
	s_addc_u32 s11, s21, 0
	s_add_i32 s46, s36, 0x1c000
	global_load_lds_dwordx4 v[6:7], off
	s_mov_b32 m0, s46
	v_lshl_add_u64 v[6:7], s[10:11], 0, v[194:195]
	s_add_i32 s47, s36, 0x1e000
	global_load_lds_dwordx4 v[6:7], off
	v_lshl_add_u64 v[6:7], s[10:11], 0, v[196:197]
	s_mov_b32 m0, s47
	v_lshl_or_b32 v218, v4, 11, v1
	global_load_lds_dwordx4 v[6:7], off
	v_and_b32_e32 v6, 15, v2
	v_bfe_u32 v4, v2, 4, 2
	v_bfe_u32 v2, v2, 1, 3
	v_lshl_or_b32 v5, v5, 11, v1
	v_lshl_or_b32 v1, s6, 6, v6
	v_bitop3_b32 v2, v3, v2, 3 bitop3:0x6c
	v_lshlrev_b32_e32 v7, 7, v1
	v_lshlrev_b32_e32 v2, 4, v2
	v_or_b32_e32 v6, s1, v6
	s_waitcnt vmcnt(10)
	s_barrier
	s_waitcnt vmcnt(6)
	v_lshlrev_b32_e32 v4, 3, v4
	v_or_b32_e32 v3, v7, v2
	v_lshlrev_b32_e32 v6, 7, v6
	v_bitop3_b32 v7, v7, 64, v2 bitop3:0x36
	s_add_u32 s10, s2, 0x30c00100
	v_add_u32_e32 v220, 0x40000, v218
	v_add_u32_e32 v200, 0x40000, v5
	v_or_b32_e32 v219, v6, v2
	v_bitop3_b32 v221, v6, 64, v2 bitop3:0x36
	v_or_b32_e32 v222, 16, v1
	v_or_b32_e32 v223, 32, v1
	v_or_b32_e32 v224, 48, v1
	v_add_u32_e32 v225, 0x80, v1
	v_add_u32_e32 v226, 0x90, v1
	v_add_u32_e32 v227, 0xa0, v1
	v_add_u32_e32 v228, 0xb0, v1
	s_addc_u32 s11, s3, 0
	v_mov_b64_e32 v[202:203], 0x400
	v_mov_b64_e32 v[204:205], 0x3ff
	s_add_i32 s48, 0, 0x10000
	s_add_i32 s49, 0, 0x14000
	s_mov_b32 s12, 0x3c800000
	s_lshl_b32 s14, s1, 1
	v_lshlrev_b32_e32 v206, 1, v4
	v_add_u32_e32 v229, 0, v3
	v_add_u32_e32 v230, 0, v7
	v_mov_b32_e32 v214, v198
	v_mov_b32_e32 v198, v5
	s_mov_b32 s6, s7
	s_barrier
	s_branch .LBB0_540

; template <class P, class MK = NoChain>
; __device__ __forceinline__ void gemm_phase(LAS unsigned char* lds, const P& p, const MK& mk = MK(), bool chain_out = false, bool chained_in = false) {
;     ...
;     int tid = threadIdx.x; asm volatile("" : "+v"(tid));
;     const int wid = __builtin_amdgcn_readfirstlane(tid >> 6), lane = tid & 63, wr = wid >> 2, wc = wid & 3, fr = lane & 15, fq = lane >> 4;
;     unsigned voffB[2], vA[2][2], nvA[2][2], nvB[2]; typedef decltype(mk()) NP; constexpr int NES = NP::FP8 ? 1 : 2; constexpr int NBMODE = bmode_of<NP>::value; constexpr size_t nhstepB = (size_t)(NBMODE == 1 ? 8 : (NBMODE == 2 ? 16 : HALF)) * NP::LDB * NES;
;     constexpr size_t kstep = (size_t)(BK * 2);
;     constexpr int BMODE = bmode_of<P>::value;
;     constexpr size_t hstep = (size_t)(BMODE == 1 ? 8 : (BMODE == 2 ? 16 : HALF)) * LDB * ES, hstepA = (size_t)HALF * LDA * ES;
; #pragma unroll
;     for (int i = 0; i < 2; ++i) { int R, C; stage_rc(tid * 16 + i * 8192, R, C); const int rho_ = R & 31;
;         const int fq_ = (rho_ & 15) >> 2, n_ = rho_ >> 4, q_ = rho_ & 3;
;         const int Rb = BMODE == 1 ? ((R >> 5) * 64 + fq_ * 16 + 4 * n_ + q_) : (BMODE == 2 ? ((R >> 5) * 64 + 32 * (fq_ >> 1) + 8 * n_ + 4 * (fq_ & 1) + q_) : (P::PERM ? ((R & ~31) + perm32(R & 31)) : R));
;         voffB[i] = (unsigned)(Rb * LDB * ES + C * 2); vA[0][i] = (unsigned)(R * LDA * ES + C * 2); vA[1][i] = vA[0][i] + (unsigned)hstepA; nvA[0][i] = vA[0][i]; nvA[1][i] = vA[1][i]; nvB[i] = voffB[i]; }
;     const unsigned ldsw = (unsigned)wid * 1024u;
;     const int aoff = lds_byte(wr * 64 + fr, fq * 8), boff = lds_byte(wc * 32 + fr, fq * 8); const int aoff1 = aoff ^ 64, boff1 = boff ^ 64;
;     ...
;     Unit cur, nxt; int ui = 0;
;     if (!p.next(0, cur)) return;
;     Acc acc;
;     if constexpr (!PEEL) {
; #pragma unroll
;     for (int a = 0; a < 2; ++a)
; #pragma unroll
;         for (int b = 0; b < 2; ++b)
; #pragma unroll
;             for (int m = 0; m < 4; ++m)
; #pragma unroll
;                 for (int n = 0; n < 2; ++n) { typedef double d2_ __attribute__((ext_vector_type(2))); d2_ z_; asm volatile("v_mov_b64 %0, 0" : "=v"(z_.x)); asm volatile("v_mov_b64 %0, 0" : "=v"(z_.y)); acc[a][b][m][n] = __builtin_bit_cast(f32x4, z_); }
;     }
;     typedef int v8i_ __attribute__((ext_vector_type(8))); typedef int v4i_ __attribute__((ext_vector_type(4)));
.LBB0_737:
	s_add_u32 s12, s0, 0x3e400000
	s_addc_u32 s13, s1, 0
	s_add_u32 s14, s0, 0x52000000
	s_addc_u32 s15, s1, 0
	s_lshl_b32 s0, s3, 5
	s_and_b32 s3, s0, 0x60
	s_add_u32 s0, s38, 0x80
	s_addc_u32 s1, s39, 0
	s_add_i32 s55, s27, 0x18000
	s_mov_b32 m0, s55
	v_lshl_add_u64 v[140:141], s[0:1], 0, v[194:195]
	s_add_i32 s56, s27, 0x1a000
	global_load_lds_dwordx4 v[140:141], off
	v_lshl_add_u64 v[140:141], s[0:1], 0, v[200:201]
	s_add_u32 s0, s30, 0x80
	s_mov_b32 m0, s56
	s_addc_u32 s1, s31, 0
	s_add_i32 s57, s27, 0x8000
	global_load_lds_dwordx4 v[140:141], off
	s_mov_b32 m0, s57
	v_lshl_add_u64 v[140:141], s[0:1], 0, v[196:197]
	s_add_i32 s58, s27, 0xa000
	global_load_lds_dwordx4 v[140:141], off
	v_lshl_add_u64 v[140:141], s[0:1], 0, v[202:203]
	s_add_u32 s0, s38, 0x40080
	s_mov_b32 m0, s58
	s_addc_u32 s1, s39, 0
	s_add_i32 s59, s27, 0x1c000
	global_load_lds_dwordx4 v[140:141], off
	s_mov_b32 m0, s59
	v_lshl_add_u64 v[140:141], s[0:1], 0, v[194:195]
	s_add_i32 s60, s27, 0x1e000
	global_load_lds_dwordx4 v[140:141], off
	v_lshl_add_u64 v[140:141], s[0:1], 0, v[200:201]
	s_mov_b32 m0, s60
	v_bfe_u32 v143, v130, 1, 3
	global_load_lds_dwordx4 v[140:141], off
	v_and_b32_e32 v141, 15, v130
	v_lshl_or_b32 v1, s2, 6, v141
	v_bitop3_b32 v139, v139, v143, 3 bitop3:0x6c
	v_or_b32_e32 v141, s3, v141
	v_lshlrev_b32_e32 v142, 7, v1
	v_lshlrev_b32_e32 v139, 4, v139
	v_lshlrev_b32_e32 v141, 7, v141
	v_bfe_u32 v140, v130, 4, 2
	v_or_b32_e32 v143, v142, v139
	v_or_b32_e32 v220, v141, v139
	v_bitop3_b32 v142, v142, 64, v139 bitop3:0x36
	v_bitop3_b32 v221, v141, 64, v139 bitop3:0x36
	v_bfe_u32 v130, v130, 3, 2
	v_lshlrev_b32_e32 v139, 2, v132
	v_and_b32_e32 v134, 0x7fffc0, v134
	v_and_or_b32 v130, v139, 48, v130
	v_or3_b32 v130, v130, v134, v135
	v_lshl_or_b32 v224, v130, 9, v131
	v_bfe_u32 v130, v136, 7, 2
	v_lshlrev_b32_e32 v134, 2, v133
	s_waitcnt vmcnt(10)
	s_barrier
	s_waitcnt vmcnt(6)
	v_lshl_or_b32 v225, v132, 9, v131
	v_and_b32_e32 v132, 0x7fffc0, v137
	v_and_or_b32 v130, v134, 48, v130
	v_lshlrev_b32_e32 v140, 3, v140
	v_or3_b32 v130, v130, v132, v138
	v_lshl_or_b32 v228, v133, 9, v131
	v_mov_b32_e32 v199, v207
	v_mov_b32_e32 v205, v207
	v_or_b32_e32 v222, s3, v140
	v_add_u32_e32 v223, 0x80, v1
	v_add_u32_e32 v226, 0x10000, v225
	v_lshl_or_b32 v227, v130, 9, v131
	v_add_u32_e32 v229, 0x10000, v228
	v_mov_b64_e32 v[208:209], 0x100
	v_mov_b64_e32 v[210:211], 0xff
	s_add_i32 s61, 0, 0x10800
	s_add_i32 s62, 0, 0x14000
	s_add_i32 s63, 0, 0x14800
	s_add_i32 s64, 0, 0x18800
	s_add_i32 s65, 0, 0x1c800
	s_lshl_b32 s16, s3, 1
	v_lshlrev_b32_e32 v212, 1, v140
	s_movk_i32 s66, 0x3000
	v_add_u32_e32 v230, 0, v143
	v_add_u32_e32 v231, 0, v142
	v_mov_b32_e32 v214, v204
	v_mov_b32_e32 v232, v198
	v_mov_b32_e32 v216, v202
	v_mov_b32_e32 v233, v196
	v_mov_b32_e32 v206, v200
	v_mov_b32_e32 v234, v194
	s_mov_b32 s10, s11
	s_barrier
	s_branch .LBB0_739

; template <class P, class MK = NoChain>
; __device__ __forceinline__ void gemm_phase(LAS unsigned char* lds, const P& p, const MK& mk = MK(), bool chain_out = false, bool chained_in = false) {
;     ...
;     int tid = threadIdx.x; asm volatile("" : "+v"(tid));
;     const int wid = __builtin_amdgcn_readfirstlane(tid >> 6), lane = tid & 63, wr = wid >> 2, wc = wid & 3, fr = lane & 15, fq = lane >> 4;
;     unsigned voffB[2], vA[2][2], nvA[2][2], nvB[2]; typedef decltype(mk()) NP; constexpr int NES = NP::FP8 ? 1 : 2; constexpr int NBMODE = bmode_of<NP>::value; constexpr size_t nhstepB = (size_t)(NBMODE == 1 ? 8 : (NBMODE == 2 ? 16 : HALF)) * NP::LDB * NES;
;     constexpr size_t kstep = (size_t)(BK * 2);
;     constexpr int BMODE = bmode_of<P>::value;
;     constexpr size_t hstep = (size_t)(BMODE == 1 ? 8 : (BMODE == 2 ? 16 : HALF)) * LDB * ES, hstepA = (size_t)HALF * LDA * ES;
; #pragma unroll
;     for (int i = 0; i < 2; ++i) { int R, C; stage_rc(tid * 16 + i * 8192, R, C); const int rho_ = R & 31;
;         const int fq_ = (rho_ & 15) >> 2, n_ = rho_ >> 4, q_ = rho_ & 3;
;         const int Rb = BMODE == 1 ? ((R >> 5) * 64 + fq_ * 16 + 4 * n_ + q_) : (BMODE == 2 ? ((R >> 5) * 64 + 32 * (fq_ >> 1) + 8 * n_ + 4 * (fq_ & 1) + q_) : (P::PERM ? ((R & ~31) + perm32(R & 31)) : R));
;         voffB[i] = (unsigned)(Rb * LDB * ES + C * 2); vA[0][i] = (unsigned)(R * LDA * ES + C * 2); vA[1][i] = vA[0][i] + (unsigned)hstepA; nvA[0][i] = vA[0][i]; nvA[1][i] = vA[1][i]; nvB[i] = voffB[i]; }
;     const unsigned ldsw = (unsigned)wid * 1024u;
;     const int aoff = lds_byte(wr * 64 + fr, fq * 8), boff = lds_byte(wc * 32 + fr, fq * 8); const int aoff1 = aoff ^ 64, boff1 = boff ^ 64;
;     ...
;     Unit cur, nxt; int ui = 0;
;     if (!p.next(0, cur)) return;
;     Acc acc;
;     if constexpr (!PEEL) {
; #pragma unroll
;     for (int a = 0; a < 2; ++a)
; #pragma unroll
;         for (int b = 0; b < 2; ++b)
; #pragma unroll
;             for (int m = 0; m < 4; ++m)
; #pragma unroll
;                 for (int n = 0; n < 2; ++n) { typedef double d2_ __attribute__((ext_vector_type(2))); d2_ z_; asm volatile("v_mov_b64 %0, 0" : "=v"(z_.x)); asm volatile("v_mov_b64 %0, 0" : "=v"(z_.y)); acc[a][b][m][n] = __builtin_bit_cast(f32x4, z_); }
;     }
;     typedef int v8i_ __attribute__((ext_vector_type(8))); typedef int v4i_ __attribute__((ext_vector_type(4)));
.LBB0_1155:
	s_add_u32 s6, s2, 0x3e400000
	s_addc_u32 s7, s3, 0
	s_add_u32 s8, s2, 0x52000000
	s_addc_u32 s9, s3, 0
	s_add_u32 s10, s2, 0x36400000
	s_addc_u32 s11, s3, 0
	s_lshl_b32 s12, s12, 5
	s_and_b32 s14, s12, 0x60
	s_add_u32 s12, s24, 0x80
	s_addc_u32 s13, s25, 0
	s_add_i32 s45, s23, 0x18000
	s_mov_b32 m0, s45
	v_lshl_add_u64 v[6:7], s[12:13], 0, v[194:195]
	s_add_i32 s46, s23, 0x1a000
	global_load_lds_dwordx4 v[6:7], off
	v_lshl_add_u64 v[6:7], s[12:13], 0, v[196:197]
	s_add_u32 s12, s2, 0x35400080
	s_mov_b32 m0, s46
	s_addc_u32 s13, s3, 0
	s_add_i32 s47, s23, 0x8000
	global_load_lds_dwordx4 v[6:7], off
	s_mov_b32 m0, s47
	v_lshl_add_u64 v[6:7], s[12:13], 0, v[198:199]
	s_add_i32 s48, s23, 0xa000
	global_load_lds_dwordx4 v[6:7], off
	v_lshl_add_u64 v[6:7], s[12:13], 0, v[206:207]
	s_add_u32 s12, s24, 0x40080
	s_mov_b32 m0, s48
	s_addc_u32 s13, s25, 0
	s_add_i32 s49, s23, 0x1c000
	global_load_lds_dwordx4 v[6:7], off
	s_mov_b32 m0, s49
	v_lshl_add_u64 v[6:7], s[12:13], 0, v[194:195]
	s_add_i32 s50, s23, 0x1e000
	global_load_lds_dwordx4 v[6:7], off
	v_lshl_add_u64 v[6:7], s[12:13], 0, v[196:197]
	s_mov_b32 m0, s50
	v_lshl_or_b32 v216, v4, 11, v1
	global_load_lds_dwordx4 v[6:7], off
	v_lshl_or_b32 v4, v5, 11, v1
	v_and_b32_e32 v5, 15, v2
	v_bfe_u32 v6, v2, 4, 2
	v_bfe_u32 v2, v2, 1, 3
	v_lshl_or_b32 v1, s4, 6, v5
	v_bitop3_b32 v2, v3, v2, 3 bitop3:0x6c
	v_lshlrev_b32_e32 v7, 7, v1
	v_lshlrev_b32_e32 v2, 4, v2
	v_or_b32_e32 v5, s14, v5
	s_waitcnt vmcnt(10)
	s_barrier
	s_waitcnt vmcnt(6)
	v_or_b32_e32 v3, v7, v2
	v_lshlrev_b32_e32 v5, 7, v5
	v_bitop3_b32 v7, v7, 64, v2 bitop3:0x36
	s_add_u32 s12, s2, 0x35400100
	v_add_u32_e32 v219, 0x40000, v216
	v_add_u32_e32 v200, 0x40000, v4
	v_or_b32_e32 v217, v5, v2
	v_bitop3_b32 v218, v5, 64, v2 bitop3:0x36
	v_add_u32_e32 v220, 0x80, v1
	v_lshl_or_b32 v221, v6, 3, s14
	s_addc_u32 s13, s3, 0
	v_mov_b64_e32 v[202:203], 0x100
	v_mov_b64_e32 v[204:205], 0xff
	s_add_i32 s51, 0, 0x10000
	s_add_i32 s52, 0, 0x14000
	s_mov_b64 s[14:15], 0x2000
	s_mov_b32 s16, 0x3c800000
	v_add_u32_e32 v222, 0, v3
	v_add_u32_e32 v223, 0, v7
	v_mov_b32_e32 v212, v198
	v_mov_b32_e32 v198, v4
	s_mov_b32 s4, s5
	s_barrier
	s_branch .LBB0_1157

; template <class P, class MK = NoChain>
; __device__ __forceinline__ void gemm_phase(LAS unsigned char* lds, const P& p, const MK& mk = MK(), bool chain_out = false, bool chained_in = false) {
;     ...
;     int tid = threadIdx.x; asm volatile("" : "+v"(tid));
;     const int wid = __builtin_amdgcn_readfirstlane(tid >> 6), lane = tid & 63, wr = wid >> 2, wc = wid & 3, fr = lane & 15, fq = lane >> 4;
;     unsigned voffB[2], vA[2][2], nvA[2][2], nvB[2]; typedef decltype(mk()) NP; constexpr int NES = NP::FP8 ? 1 : 2; constexpr int NBMODE = bmode_of<NP>::value; constexpr size_t nhstepB = (size_t)(NBMODE == 1 ? 8 : (NBMODE == 2 ? 16 : HALF)) * NP::LDB * NES;
;     constexpr size_t kstep = (size_t)(BK * 2);
;     constexpr int BMODE = bmode_of<P>::value;
;     constexpr size_t hstep = (size_t)(BMODE == 1 ? 8 : (BMODE == 2 ? 16 : HALF)) * LDB * ES, hstepA = (size_t)HALF * LDA * ES;
; #pragma unroll
;     for (int i = 0; i < 2; ++i) { int R, C; stage_rc(tid * 16 + i * 8192, R, C); const int rho_ = R & 31;
;         const int fq_ = (rho_ & 15) >> 2, n_ = rho_ >> 4, q_ = rho_ & 3;
;         const int Rb = BMODE == 1 ? ((R >> 5) * 64 + fq_ * 16 + 4 * n_ + q_) : (BMODE == 2 ? ((R >> 5) * 64 + 32 * (fq_ >> 1) + 8 * n_ + 4 * (fq_ & 1) + q_) : (P::PERM ? ((R & ~31) + perm32(R & 31)) : R));
;         voffB[i] = (unsigned)(Rb * LDB * ES + C * 2); vA[0][i] = (unsigned)(R * LDA * ES + C * 2); vA[1][i] = vA[0][i] + (unsigned)hstepA; nvA[0][i] = vA[0][i]; nvA[1][i] = vA[1][i]; nvB[i] = voffB[i]; }
;     const unsigned ldsw = (unsigned)wid * 1024u;
;     const int aoff = lds_byte(wr * 64 + fr, fq * 8), boff = lds_byte(wc * 32 + fr, fq * 8); const int aoff1 = aoff ^ 64, boff1 = boff ^ 64;
;     ...
;     Unit cur, nxt; int ui = 0;
;     if (!p.next(0, cur)) return;
;     Acc acc;
;     if constexpr (!PEEL) {
; #pragma unroll
;     for (int a = 0; a < 2; ++a)
; #pragma unroll
;         for (int b = 0; b < 2; ++b)
; #pragma unroll
;             for (int m = 0; m < 4; ++m)
; #pragma unroll
;                 for (int n = 0; n < 2; ++n) { typedef double d2_ __attribute__((ext_vector_type(2))); d2_ z_; asm volatile("v_mov_b64 %0, 0" : "=v"(z_.x)); asm volatile("v_mov_b64 %0, 0" : "=v"(z_.y)); acc[a][b][m][n] = __builtin_bit_cast(f32x4, z_); }
;     }
;     typedef int v8i_ __attribute__((ext_vector_type(8))); typedef int v4i_ __attribute__((ext_vector_type(4)));
.LBB0_1251:
	s_add_u32 s8, s2, 0x38400000
	s_addc_u32 s9, s3, 0
	s_add_u32 s44, s2, 0x14000
	s_addc_u32 s45, s3, 0
	s_lshl_b32 s10, s10, 5
	s_and_b32 s12, s10, 0x60
	s_add_u32 s10, s22, 0x80
	s_addc_u32 s11, s23, 0
	s_add_i32 s46, s38, 0x18000
	s_mov_b32 m0, s46
	v_lshl_add_u64 v[4:5], s[10:11], 0, v[194:195]
	s_add_i32 s47, s38, 0x1a000
	global_load_lds_dwordx4 v[4:5], off
	v_lshl_add_u64 v[4:5], s[10:11], 0, v[196:197]
	s_add_u32 s10, s2, 0x36400080
	s_mov_b32 m0, s47
	s_addc_u32 s11, s3, 0
	s_add_i32 s48, s38, 0x8000
	global_load_lds_dwordx4 v[4:5], off
	s_mov_b32 m0, s48
	v_lshl_add_u64 v[4:5], s[10:11], 0, v[198:199]
	s_add_i32 s49, s38, 0xa000
	global_load_lds_dwordx4 v[4:5], off
	v_lshl_add_u64 v[4:5], s[10:11], 0, v[208:209]
	s_add_u32 s10, s22, 0x40080
	s_mov_b32 m0, s49
	s_addc_u32 s11, s23, 0
	s_add_i32 s50, s38, 0x1c000
	global_load_lds_dwordx4 v[4:5], off
	s_mov_b32 m0, s50
	v_lshl_add_u64 v[4:5], s[10:11], 0, v[194:195]
	s_add_i32 s51, s38, 0x1e000
	global_load_lds_dwordx4 v[4:5], off
	v_lshl_add_u64 v[4:5], s[10:11], 0, v[196:197]
	s_mov_b32 m0, s51
	v_lshrrev_b32_e32 v3, 4, v2
	global_load_lds_dwordx4 v[4:5], off
	v_and_b32_e32 v4, 15, v2
	v_bfe_u32 v5, v2, 4, 2
	v_bfe_u32 v2, v2, 1, 3
	v_lshl_or_b32 v1, s6, 6, v4
	v_bitop3_b32 v2, v3, v2, 3 bitop3:0x6c
	v_or_b32_e32 v4, s12, v4
	v_lshlrev_b32_e32 v6, 7, v1
	v_lshlrev_b32_e32 v2, 4, v2
	v_lshlrev_b32_e32 v4, 7, v4
	s_waitcnt vmcnt(10)
	s_barrier
	s_waitcnt vmcnt(6)
	v_or_b32_e32 v3, v6, v2
	v_or_b32_e32 v218, v4, v2
	v_bitop3_b32 v6, v6, 64, v2 bitop3:0x36
	v_bitop3_b32 v219, v4, 64, v2 bitop3:0x36
	v_lshlrev_b32_e32 v2, 2, v5
	s_add_u32 s10, s2, 0x36400100
	v_add_u32_e32 v220, 0x40000, v194
	v_add_u32_e32 v200, 0x40000, v196
	v_or_b32_e32 v221, s12, v2
	v_add_u32_e32 v222, 0x80, v1
	s_addc_u32 s11, s3, 0
	v_mov_b64_e32 v[202:203], 0x100
	v_mov_b64_e32 v[204:205], 0xff
	s_add_i32 s52, 0, 0x10000
	s_add_i32 s53, 0, 0x14000
	s_lshl_b32 s12, s12, 2
	v_lshlrev_b32_e32 v206, 2, v2
	s_mov_b32 s14, 0x3c800000
	v_add_u32_e32 v223, 0, v3
	v_add_u32_e32 v224, 0, v6
	v_mov_b32_e32 v214, v198
	v_mov_b32_e32 v198, v196
	v_mov_b32_e32 v225, v194
	s_mov_b32 s6, s7
	s_barrier
	s_branch .LBB0_1253

; template <class P, class MK = NoChain>
; __device__ __forceinline__ void gemm_phase(LAS unsigned char* lds, const P& p, const MK& mk = MK(), bool chain_out = false, bool chained_in = false) {
;     ...
;     int tid = threadIdx.x; asm volatile("" : "+v"(tid));
;     const int wid = __builtin_amdgcn_readfirstlane(tid >> 6), lane = tid & 63, wr = wid >> 2, wc = wid & 3, fr = lane & 15, fq = lane >> 4;
;     unsigned voffB[2], vA[2][2], nvA[2][2], nvB[2]; typedef decltype(mk()) NP; constexpr int NES = NP::FP8 ? 1 : 2; constexpr int NBMODE = bmode_of<NP>::value; constexpr size_t nhstepB = (size_t)(NBMODE == 1 ? 8 : (NBMODE == 2 ? 16 : HALF)) * NP::LDB * NES;
;     constexpr size_t kstep = (size_t)(BK * 2);
;     constexpr int BMODE = bmode_of<P>::value;
;     constexpr size_t hstep = (size_t)(BMODE == 1 ? 8 : (BMODE == 2 ? 16 : HALF)) * LDB * ES, hstepA = (size_t)HALF * LDA * ES;
; #pragma unroll
;     for (int i = 0; i < 2; ++i) { int R, C; stage_rc(tid * 16 + i * 8192, R, C); const int rho_ = R & 31;
;         const int fq_ = (rho_ & 15) >> 2, n_ = rho_ >> 4, q_ = rho_ & 3;
;         const int Rb = BMODE == 1 ? ((R >> 5) * 64 + fq_ * 16 + 4 * n_ + q_) : (BMODE == 2 ? ((R >> 5) * 64 + 32 * (fq_ >> 1) + 8 * n_ + 4 * (fq_ & 1) + q_) : (P::PERM ? ((R & ~31) + perm32(R & 31)) : R));
;         voffB[i] = (unsigned)(Rb * LDB * ES + C * 2); vA[0][i] = (unsigned)(R * LDA * ES + C * 2); vA[1][i] = vA[0][i] + (unsigned)hstepA; nvA[0][i] = vA[0][i]; nvA[1][i] = vA[1][i]; nvB[i] = voffB[i]; }
;     const unsigned ldsw = (unsigned)wid * 1024u;
;     const int aoff = lds_byte(wr * 64 + fr, fq * 8), boff = lds_byte(wc * 32 + fr, fq * 8); const int aoff1 = aoff ^ 64, boff1 = boff ^ 64;
;     ...
;     Unit cur, nxt; int ui = 0;
;     if (!p.next(0, cur)) return;
;     Acc acc;
;     if constexpr (!PEEL) {
; #pragma unroll
;     for (int a = 0; a < 2; ++a)
; #pragma unroll
;         for (int b = 0; b < 2; ++b)
; #pragma unroll
;             for (int m = 0; m < 4; ++m)
; #pragma unroll
;                 for (int n = 0; n < 2; ++n) { typedef double d2_ __attribute__((ext_vector_type(2))); d2_ z_; asm volatile("v_mov_b64 %0, 0" : "=v"(z_.x)); asm volatile("v_mov_b64 %0, 0" : "=v"(z_.y)); acc[a][b][m][n] = __builtin_bit_cast(f32x4, z_); }
;     }
;     typedef int v8i_ __attribute__((ext_vector_type(8))); typedef int v4i_ __attribute__((ext_vector_type(4)));
.LBB0_1466:
	s_lshl_b32 s1, s1, 5
	s_and_b32 s10, s1, 0x60
	s_add_u32 s2, s34, 0x80
	s_addc_u32 s3, s35, 0
	s_add_i32 s58, s52, 0x18000
	s_add_i32 s59, s52, 0x1a000
	s_add_u32 s12, s14, 0x30c00080
	s_mov_b32 m0, s58
	v_lshl_add_u64 v[6:7], s[2:3], 0, v[212:213]
	s_addc_u32 s13, s15, 0
	global_load_lds_dwordx4 v[6:7], off
	v_lshl_add_u64 v[6:7], s[2:3], 0, v[214:215]
	s_mov_b32 m0, s59
	s_mov_b64 s[2:3], s[12:13]
	s_add_i32 s60, s52, 0x8000
	global_load_lds_dwordx4 v[6:7], off
	s_mov_b32 m0, s60
	v_lshl_add_u64 v[6:7], s[2:3], 0, v[210:211]
	s_add_i32 s61, s52, 0xa000
	global_load_lds_dwordx4 v[6:7], off
	v_lshl_add_u64 v[6:7], s[2:3], 0, v[220:221]
	s_add_u32 s2, s34, 0x40080
	s_mov_b32 m0, s61
	s_addc_u32 s3, s35, 0
	s_add_i32 s62, s52, 0x1c000
	global_load_lds_dwordx4 v[6:7], off
	s_mov_b32 m0, s62
	v_lshl_add_u64 v[6:7], s[2:3], 0, v[212:213]
	s_add_i32 s63, s52, 0x1e000
	global_load_lds_dwordx4 v[6:7], off
	v_lshl_add_u64 v[6:7], s[2:3], 0, v[214:215]
	s_mov_b32 m0, s63
	s_add_u32 s16, s14, 0x30c00100
	global_load_lds_dwordx4 v[6:7], off
	s_addc_u32 s17, s15, 0
	v_lshl_or_b32 v240, v4, 11, v3
	v_and_b32_e32 v4, 15, v11
	v_bfe_u32 v6, v11, 1, 3
	s_add_u32 s18, s14, 0x30c00180
	v_lshl_or_b32 v3, v5, 11, v3
	v_bfe_u32 v5, v11, 4, 2
	v_lshl_or_b32 v228, s0, 6, v4
	v_bitop3_b32 v2, v2, v6, 3 bitop3:0x6c
	s_addc_u32 s19, s15, 0
	v_lshlrev_b32_e32 v216, 3, v5
	v_lshlrev_b32_e32 v5, 7, v228
	v_lshlrev_b32_e32 v2, 4, v2
	v_or_b32_e32 v4, s10, v4
	s_waitcnt vmcnt(10)
	s_barrier
	s_waitcnt vmcnt(6)
	s_add_u32 s20, s14, 0x30c00200
	v_or_b32_e32 v6, v5, v2
	v_lshlrev_b32_e32 v4, 7, v4
	v_bitop3_b32 v5, v5, 64, v2 bitop3:0x36
	s_addc_u32 s21, s15, 0
	s_add_i32 s0, 0, 0x20400
	v_add_u32_e32 v241, 0x40000, v240
	v_add_u32_e32 v218, 0x40000, v3
	v_or_b32_e32 v229, v4, v2
	v_bitop3_b32 v230, v4, 64, v2 bitop3:0x36
	v_mov_b32_e32 v217, v211
	v_or_b32_e32 v231, 16, v228
	v_or_b32_e32 v232, 32, v228
	v_or_b32_e32 v233, 48, v228
	v_mov_b32_e32 v234, s0
	s_add_i32 s64, 0, 0x10000
	s_add_i32 s65, 0, 0x14000
	s_mov_b32 s66, 0x3f100000
	s_mov_b32 s22, 0x3c800000
	v_add_u32_e32 v235, 0, v6
	v_add_u32_e32 v236, 0, v5
	v_mov_b32_e32 v226, v210
	v_mov_b32_e32 v210, v3
	s_mov_b32 s67, s11
	s_barrier
	s_branch .LBB0_1469

; #define LAS __attribute__((address_space(3)))
; __device__ __forceinline__ int otid() { int t = threadIdx.x; asm volatile("" : "+v"(t)); return t; }
; #define REP(k) for (int rep_ = 0; rep_ < ((REP_KIND == (k)) ? REP_N : 1); ++rep_)
; #define IN(k) (fresh_args()->ph_lo <= (k) && (k) < fresh_args()->ph_hi)
; #define PHASE_ARGS() CArgs* A_p = fresh_args(); CArgs& A = *A_p; unsigned char* ws = A.ws; (void)ws;
; __device__ __forceinline__ MoeTab moe_tables(CArgs& A, int l, LAS unsigned char* lds, bool want_order) {
;     MoeTab T; T.cnt = (LAS int*)(lds + LDS_TAB + 256); T.ts = T.cnt + 64; T.ord = (LAS int*)(lds + LDS_TAB + 1024) + 1;
;     unsigned* cg = (unsigned*)(A.ws + WS_CTL) + CW_CNT + l * 64;
;     const int tt = otid();
;     __syncthreads();
;     if (tt < 64) {
;         const int e = tt; const int c = (int)__hip_atomic_load(cg + e, RLX_AGENT);
;         T.cnt[e] = c;
;         const int nall = (c + 255) >> 8; const int ia = wave_incl_scan(nall, e);
;         T.ts[e] = ia - nall; if (e == 63) T.ts[64] = ia;
;         if (want_order) {
;             const int nfull = c >> 8, rem = c & 255;
;             const int n1 = nfull + (rem > 128 ? 1 : 0), nh = (rem != 0 && rem <= 128) ? 1 : 0;
;             const int p1 = wave_incl_scan(n1, e), ph = wave_incl_scan(nh, e);
;             const int tot1 = __builtin_amdgcn_readlane(p1, 63), toth = __builtin_amdgcn_readlane(ph, 63);
;             if (e < NT / 256) T.ord[e] = 64 | (e << 8);
;             const int pos = NT / 256 + p1 - n1;
; #pragma nounroll
;             for (int m = 0; m < n1; ++m) T.ord[pos + m] = e | (m << 8);
;             if (nh) T.ord[NT / 256 + tot1 + ph - 1] = e | (nfull << 8) | (1 << 16);
;             if (e == 0) T.ord[-1] = NT / 256 + tot1 + toth;
;         }
;     }
;     __syncthreads();
;     return T;
; }
; template <int l> __device__ __forceinline__ void layer_body(LAS unsigned char* lds, unsigned char* lds_raw, int bx, int vcu) {
;     ...
;         if (KEN(10) && IN(pb + 8)) REP(10) { PHASE_ARGS();
;             Moe2P P; P.ACT = (const char*)(ws + WS_ACT); P.SACT = (const char*)(ws + WS_SACT); P.W = (const char*)(ws + WS_W2E) + (size_t)l * NE * DM * DE; P.WS2 = (const char*)(ws + WS_W2S) + (size_t)l * DM * DS;
;             P.OUT2 = (bf16*)(ws + WS_OUT2); P.T = moe_tables(A, l, lds, true); P.G = G; P.c = bx;
.LBB0_1593:
	s_mov_b64 s[0:1], s[24:25]
	s_mov_b32 s0, s100
	s_waitcnt lgkmcnt(0)
	s_cmp_gt_i32 s0, 10
	s_cbranch_scc1 .LBB0_1669
	s_mov_b64 s[0:1], s[24:25]
	s_mov_b32 s0, s101
	s_waitcnt lgkmcnt(0)
	s_cmp_lt_i32 s0, 11
	s_cbranch_scc1 .LBB0_1669
	s_mov_b64 s[0:1], s[24:25]
	s_mov_b64 s[14:15], s[98:99]
	v_mov_b32_e32 v2, v0
	s_waitcnt vmcnt(0) lgkmcnt(0)
	s_mov_b64 vcc, 0
	s_barrier
	s_and_saveexec_b64 s[16:17], vcc
	s_cbranch_execz .LBB0_1614
	v_ashrrev_i32_e32 v3, 31, v2
	v_mul_u32_u24_e32 v4, 0x1100, v2
	v_mov_b32_e32 v5, 0
	v_lshl_add_u64 v[4:5], v[4:5], 0, s[14:15]
	v_add_co_u32_e32 v4, vcc, 0x80000, v4
	v_cmp_lt_i32_e64 s[0:1], 0, v2
	s_nop 0
	v_addc_co_u32_e32 v5, vcc, 0, v5, vcc
	global_load_dword v3, v[4:5], off sc1
	v_mbcnt_lo_u32_b32 v4, -1, 0
	v_mbcnt_hi_u32_b32 v4, -1, v4
	v_and_b32_e32 v10, 64, v4
	v_add_u32_e32 v5, -1, v4
	v_cmp_lt_i32_e32 vcc, v5, v10
	v_add_u32_e32 v6, -2, v4
	v_add_u32_e32 v7, -4, v4
	v_cndmask_b32_e32 v5, v5, v4, vcc
	v_lshlrev_b32_e32 v5, 2, v5
	v_cmp_lt_i32_e32 vcc, v6, v10
	v_cmp_gt_i32_e64 s[2:3], 2, v2
	v_add_u32_e32 v8, -8, v4
	v_cndmask_b32_e32 v6, v6, v4, vcc
	v_lshlrev_b32_e32 v6, 2, v6
	v_cmp_lt_i32_e32 vcc, v7, v10
	v_cmp_gt_i32_e64 s[4:5], 4, v2
	v_add_u32_e32 v9, -16, v4
	v_cndmask_b32_e32 v7, v7, v4, vcc
	v_lshlrev_b32_e32 v7, 2, v7
	v_cmp_lt_i32_e32 vcc, v8, v10
	v_cmp_gt_i32_e64 s[6:7], 8, v2
	v_subrev_u32_e32 v11, 32, v4
	v_cndmask_b32_e32 v8, v8, v4, vcc
	v_lshlrev_b32_e32 v8, 2, v8
	v_cmp_lt_i32_e32 vcc, v9, v10
	v_cmp_gt_i32_e64 s[8:9], 16, v2
	v_cmp_gt_i32_e64 s[10:11], 32, v2
	v_cndmask_b32_e32 v9, v9, v4, vcc
	v_lshlrev_b32_e32 v9, 2, v9
	v_cmp_lt_i32_e32 vcc, v11, v10
	v_lshl_add_u32 v1, v2, 2, 0
	s_waitcnt vmcnt(0)
	v_add_u32_e32 v12, 0xff, v3
	v_ashrrev_i32_e32 v12, 8, v12
	ds_bpermute_b32 v13, v5, v12
	v_cndmask_b32_e32 v4, v11, v4, vcc
	v_lshlrev_b32_e32 v10, 2, v4
	v_cmp_eq_u32_e32 vcc, 63, v2
	s_waitcnt lgkmcnt(0)
	v_cndmask_b32_e64 v13, 0, v13, s[0:1]
	v_add_u32_e32 v13, v13, v12
	ds_bpermute_b32 v14, v6, v13
	s_waitcnt lgkmcnt(0)
	v_cndmask_b32_e64 v14, v14, 0, s[2:3]
	v_add_u32_e32 v13, v14, v13
	ds_bpermute_b32 v14, v7, v13
	s_waitcnt lgkmcnt(0)
	v_cndmask_b32_e64 v14, v14, 0, s[4:5]
	v_add_u32_e32 v13, v14, v13
	ds_bpermute_b32 v14, v8, v13
	s_waitcnt lgkmcnt(0)
	v_cndmask_b32_e64 v14, v14, 0, s[6:7]
	v_add_u32_e32 v13, v14, v13
	ds_bpermute_b32 v14, v9, v13
	s_waitcnt lgkmcnt(0)
	v_cndmask_b32_e64 v4, v14, 0, s[8:9]
	v_add_u32_e32 v4, v4, v13
	ds_bpermute_b32 v11, v10, v4
	v_add_u32_e32 v13, 0x20100, v1
	v_add_u32_e32 v14, 0x20200, v1
	ds_write_b32 v13, v3
	s_waitcnt lgkmcnt(1)
	v_cndmask_b32_e64 v11, v11, 0, s[10:11]
	v_add_u32_e32 v4, v11, v4
	v_sub_u32_e32 v11, v4, v12
	ds_write_b32 v14, v11
	s_and_saveexec_b64 s[12:13], vcc
	s_add_i32 s18, 0, 0x20300
	v_mov_b32_e32 v11, s18
	ds_write_b32 v11, v4
	s_or_b64 exec, exec, s[12:13]
	s_movk_i32 s18, 0x80
	v_ashrrev_i32_e32 v12, 8, v3
	v_cmp_gt_u32_sdwa s[12:13], v3, s18 src0_sel:BYTE_0 src1_sel:DWORD
	v_mov_b32_e32 v11, -1
	v_add_u32_sdwa v11, v3, v11 dst_sel:DWORD dst_unused:UNUSED_PAD src0_sel:BYTE_0 src1_sel:DWORD
	v_addc_co_u32_e64 v4, vcc, 0, v12, s[12:13]
	v_cmp_gt_u32_e32 vcc, s18, v11
	ds_bpermute_b32 v13, v5, v4
	s_nop 0
	v_cndmask_b32_e64 v11, 0, 1, vcc
	ds_bpermute_b32 v5, v5, v11
	s_waitcnt lgkmcnt(1)
	v_cndmask_b32_e64 v11, 0, v13, s[0:1]
	v_addc_co_u32_e64 v12, s[12:13], v11, v12, s[12:13]
	s_waitcnt lgkmcnt(0)
	v_cndmask_b32_e64 v5, 0, v5, s[0:1]
	v_addc_co_u32_e64 v14, s[0:1], 0, v5, vcc
	ds_bpermute_b32 v13, v6, v12
	ds_bpermute_b32 v14, v6, v14
	s_waitcnt lgkmcnt(1)
	v_cndmask_b32_e64 v6, v13, 0, s[2:3]
	s_waitcnt lgkmcnt(0)
	v_cndmask_b32_e64 v14, v14, 0, s[2:3]
	v_add_u32_e32 v12, v6, v12
	v_addc_co_u32_e64 v5, s[0:1], v14, v5, vcc
	ds_bpermute_b32 v13, v7, v12
	ds_bpermute_b32 v14, v7, v5
	s_waitcnt lgkmcnt(1)
	v_cndmask_b32_e64 v7, v13, 0, s[4:5]
	s_waitcnt lgkmcnt(0)
	v_cndmask_b32_e64 v14, v14, 0, s[4:5]
	v_add_u32_e32 v13, v7, v12
	v_add_u32_e32 v5, v14, v5
	ds_bpermute_b32 v12, v8, v13
	ds_bpermute_b32 v8, v8, v5
	s_waitcnt lgkmcnt(1)
	v_cndmask_b32_e64 v12, v12, 0, s[6:7]
	s_waitcnt lgkmcnt(0)
	v_cndmask_b32_e64 v8, v8, 0, s[6:7]
	v_add_u32_e32 v13, v12, v13
	v_add_u32_e32 v5, v8, v5
	ds_bpermute_b32 v14, v9, v13
	ds_bpermute_b32 v8, v9, v5
	s_waitcnt lgkmcnt(1)
	v_cndmask_b32_e64 v9, v14, 0, s[8:9]
	s_waitcnt lgkmcnt(0)
	v_cndmask_b32_e64 v8, v8, 0, s[8:9]
	v_add_u32_e32 v13, v9, v13
	v_add_u32_e32 v5, v8, v5
	ds_bpermute_b32 v14, v10, v13
	ds_bpermute_b32 v10, v10, v5
	s_waitcnt lgkmcnt(1)
	v_cndmask_b32_e64 v8, v14, 0, s[10:11]
	s_waitcnt lgkmcnt(0)
	v_cndmask_b32_e64 v10, v10, 0, s[10:11]
	v_add_u32_e32 v13, v8, v13
	v_add_u32_e32 v5, v10, v5
	v_readlane_b32 s8, v13, 63
	v_readlane_b32 s9, v5, 63
	s_and_saveexec_b64 s[0:1], s[10:11]
	v_add_u32_e32 v1, 0x20404, v1
	v_lshl_or_b32 v10, v2, 8, 64
	ds_write_b32 v1, v10
	s_or_b64 exec, exec, s[0:1]
	v_cmp_lt_i32_e64 s[0:1], 0, v4
	s_and_saveexec_b64 s[2:3], s[0:1]
	s_cbranch_execz .LBB0_1610
	v_add3_u32 v1, v11, v6, v7
	s_mov_b32 s10, 1
	v_cmp_ne_u32_e64 s[0:1], 1, v4
	s_mov_b64 s[6:7], 0
	v_add3_u32 v9, v1, v12, v9
	s_and_saveexec_b64 s[4:5], s[0:1]
	s_xor_b64 s[4:5], exec, s[4:5]
	s_cbranch_execnz .LBB0_1604
	s_andn2_saveexec_b64 s[0:1], s[4:5]
	s_cbranch_execnz .LBB0_1607

; template <class P, class MK = NoChain>
; __device__ __forceinline__ void gemm_phase(LAS unsigned char* lds, const P& p, const MK& mk = MK(), bool chain_out = false, bool chained_in = false) {
;     ...
;     int tid = threadIdx.x; asm volatile("" : "+v"(tid));
;     const int wid = __builtin_amdgcn_readfirstlane(tid >> 6), lane = tid & 63, wr = wid >> 2, wc = wid & 3, fr = lane & 15, fq = lane >> 4;
;     unsigned voffB[2], vA[2][2], nvA[2][2], nvB[2]; typedef decltype(mk()) NP; constexpr int NES = NP::FP8 ? 1 : 2; constexpr int NBMODE = bmode_of<NP>::value; constexpr size_t nhstepB = (size_t)(NBMODE == 1 ? 8 : (NBMODE == 2 ? 16 : HALF)) * NP::LDB * NES;
;     constexpr size_t kstep = (size_t)(BK * 2);
;     constexpr int BMODE = bmode_of<P>::value;
;     constexpr size_t hstep = (size_t)(BMODE == 1 ? 8 : (BMODE == 2 ? 16 : HALF)) * LDB * ES, hstepA = (size_t)HALF * LDA * ES;
; #pragma unroll
;     for (int i = 0; i < 2; ++i) { int R, C; stage_rc(tid * 16 + i * 8192, R, C); const int rho_ = R & 31;
;         const int fq_ = (rho_ & 15) >> 2, n_ = rho_ >> 4, q_ = rho_ & 3;
;         const int Rb = BMODE == 1 ? ((R >> 5) * 64 + fq_ * 16 + 4 * n_ + q_) : (BMODE == 2 ? ((R >> 5) * 64 + 32 * (fq_ >> 1) + 8 * n_ + 4 * (fq_ & 1) + q_) : (P::PERM ? ((R & ~31) + perm32(R & 31)) : R));
;         voffB[i] = (unsigned)(Rb * LDB * ES + C * 2); vA[0][i] = (unsigned)(R * LDA * ES + C * 2); vA[1][i] = vA[0][i] + (unsigned)hstepA; nvA[0][i] = vA[0][i]; nvA[1][i] = vA[1][i]; nvB[i] = voffB[i]; }
;     const unsigned ldsw = (unsigned)wid * 1024u;
;     const int aoff = lds_byte(wr * 64 + fr, fq * 8), boff = lds_byte(wc * 32 + fr, fq * 8); const int aoff1 = aoff ^ 64, boff1 = boff ^ 64;
;     ...
;     Unit cur, nxt; int ui = 0;
;     if (!p.next(0, cur)) return;
;     Acc acc;
;     if constexpr (!PEEL) {
; #pragma unroll
;     for (int a = 0; a < 2; ++a)
; #pragma unroll
;         for (int b = 0; b < 2; ++b)
; #pragma unroll
;             for (int m = 0; m < 4; ++m)
; #pragma unroll
;                 for (int n = 0; n < 2; ++n) { typedef double d2_ __attribute__((ext_vector_type(2))); d2_ z_; asm volatile("v_mov_b64 %0, 0" : "=v"(z_.x)); asm volatile("v_mov_b64 %0, 0" : "=v"(z_.y)); acc[a][b][m][n] = __builtin_bit_cast(f32x4, z_); }
;     }
;     typedef int v8i_ __attribute__((ext_vector_type(8))); typedef int v4i_ __attribute__((ext_vector_type(4)));
.LBB0_1627:
	s_and_b32 s1, s1, 3
	s_add_u32 s10, s14, 0x44100000
	s_addc_u32 s11, s15, 0
	s_add_u32 s2, s24, 0x80
	s_addc_u32 s3, s25, 0
	s_add_i32 m0, s43, 0x18000
	v_lshl_add_u64 v[4:5], s[2:3], 0, v[226:227]
	global_load_lds_dwordx4 v[4:5], off
	s_add_i32 m0, s43, 0x1a000
	v_lshl_add_u64 v[4:5], s[2:3], 0, v[232:233]
	s_add_u32 s2, s22, 0x80
	s_addc_u32 s3, s23, 0
	s_add_i32 s50, s43, 0x8000
	global_load_lds_dwordx4 v[4:5], off
	s_mov_b32 m0, s50
	v_lshl_add_u64 v[4:5], s[2:3], 0, v[228:229]
	s_add_i32 s51, s43, 0xa000
	global_load_lds_dwordx4 v[4:5], off
	v_lshl_add_u64 v[4:5], s[2:3], 0, v[234:235]
	s_add_u32 s2, s24, 0x1080
	s_mov_b32 m0, s51
	s_addc_u32 s3, s25, 0
	s_add_i32 s52, s43, 0x1c000
	global_load_lds_dwordx4 v[4:5], off
	s_mov_b32 m0, s52
	v_lshl_add_u64 v[4:5], s[2:3], 0, v[226:227]
	s_add_i32 s53, s43, 0x1e000
	global_load_lds_dwordx4 v[4:5], off
	v_lshl_add_u64 v[4:5], s[2:3], 0, v[232:233]
	s_mov_b32 m0, s53
	v_mov_b32_e32 v231, v227
	global_load_lds_dwordx4 v[4:5], off
	v_and_b32_e32 v4, 15, v2
	v_bfe_u32 v5, v2, 4, 2
	v_bfe_u32 v2, v2, 1, 3
	v_lshl_or_b32 v1, s0, 6, v4
	v_bitop3_b32 v2, v3, v2, 3 bitop3:0x6c
	v_lshlrev_b32_e32 v6, 7, v1
	v_lshlrev_b32_e32 v2, 4, v2
	v_lshlrev_b32_e32 v4, 7, v4
	s_waitcnt vmcnt(10)
	s_barrier
	s_waitcnt vmcnt(6)
	v_or_b32_e32 v3, v6, v2
	v_lshl_or_b32 v4, s1, 12, v4
	v_bitop3_b32 v6, v6, 64, v2 bitop3:0x36
	s_add_i32 s0, 0, 0x20400
	v_mov_b32_e32 v237, v227
	v_or_b32_e32 v240, v4, v2
	v_bitop3_b32 v241, v4, 64, v2 bitop3:0x36
	s_lshl_b32 s8, s1, 6
	v_lshlrev_b32_e32 v238, 4, v5
	v_mov_b32_e32 v239, v227
	v_or_b32_e32 v243, 32, v1
	v_or_b32_e32 v244, 48, v1
	s_add_i32 s54, s12, 0x100
	v_mov_b32_e32 v245, s0
	s_add_i32 s55, 0, 0x10000
	s_mov_b32 s12, 0x3d000000
	v_add_u32_e32 v246, 0, v3
	v_add_u32_e32 v247, 0, v6
	s_barrier
	s_branch .LBB0_1629

; #define LAS __attribute__((address_space(3)))
; __device__ __forceinline__ int otid() { int t = threadIdx.x; asm volatile("" : "+v"(t)); return t; }
; __device__ __forceinline__ MoeTab moe_tables(CArgs& A, int l, LAS unsigned char* lds, bool want_order) {
;     MoeTab T; T.cnt = (LAS int*)(lds + LDS_TAB + 256); T.ts = T.cnt + 64; T.ord = (LAS int*)(lds + LDS_TAB + 1024) + 1;
;     unsigned* cg = (unsigned*)(A.ws + WS_CTL) + CW_CNT + l * 64;
;     const int tt = otid();
;     __syncthreads();
;     if (tt < 64) {
;         const int e = tt; const int c = (int)__hip_atomic_load(cg + e, RLX_AGENT);
;         T.cnt[e] = c;
;         const int nall = (c + 255) >> 8; const int ia = wave_incl_scan(nall, e);
;         T.ts[e] = ia - nall; if (e == 63) T.ts[64] = ia;
; __device__ __forceinline__ void combine_phase(CArgs& A, int l, const float* xin, LAS unsigned char* lds, int vcu, int G) {
;     int tid = threadIdx.x; asm volatile("" : "+v"(tid));
;     const int lane = tid & 63, wave = __builtin_amdgcn_readfirstlane(tid >> 6);
;     const MoeTab T = moe_tables(A, l, lds, false);
.LBB0_1727:
	s_mov_b64 s[0:1], s[24:25]
	s_mov_b32 s0, s100
	s_waitcnt lgkmcnt(0)
	s_cmp_gt_i32 s0, 11
	s_cbranch_scc1 .LBB0_1736
	s_mov_b64 s[0:1], s[24:25]
	s_mov_b32 s0, s101
	s_waitcnt lgkmcnt(0)
	s_cmp_lt_i32 s0, 12
	s_cbranch_scc1 .LBB0_1736
	s_mov_b64 s[6:7], s[24:25]
	s_mov_b64 s[0:1], s[98:99]
	v_mov_b32_e32 v1, v0
	v_mov_b32_e32 v2, v0
	s_waitcnt vmcnt(0) lgkmcnt(0)
	v_readfirstlane_b32 s4, v1
	s_mov_b64 vcc, 0
	s_barrier
	s_and_saveexec_b64 s[2:3], vcc
	s_cbranch_execz .LBB0_1732
	v_ashrrev_i32_e32 v3, 31, v2
	v_mul_u32_u24_e32 v4, 0x1100, v2
	v_mov_b32_e32 v5, 0
	v_lshl_add_u64 v[4:5], v[4:5], 0, s[0:1]
	v_add_co_u32_e32 v4, vcc, 0x80000, v4
	s_nop 1
	v_addc_co_u32_e32 v5, vcc, 0, v5, vcc
	global_load_dword v3, v[4:5], off sc1
	v_mbcnt_lo_u32_b32 v5, -1, 0
	v_mbcnt_hi_u32_b32 v5, -1, v5
	v_and_b32_e32 v6, 64, v5
	v_add_u32_e32 v7, -1, v5
	v_cmp_lt_i32_e32 vcc, v7, v6
	v_add_u32_e32 v8, -2, v5
	v_add_u32_e32 v9, -4, v5
	v_cndmask_b32_e32 v7, v7, v5, vcc
	v_lshlrev_b32_e32 v7, 2, v7
	v_cmp_lt_i32_e32 vcc, v8, v6
	v_add_u32_e32 v10, -8, v5
	v_add_u32_e32 v11, -16, v5
	v_cndmask_b32_e32 v8, v8, v5, vcc
	v_cmp_lt_i32_e32 vcc, 0, v2
	v_lshlrev_b32_e32 v8, 2, v8
	v_subrev_u32_e32 v12, 32, v5
	v_lshl_add_u32 v4, v2, 2, 0
	s_waitcnt vmcnt(0)
	v_add_u32_e32 v13, 0xff, v3
	v_ashrrev_i32_e32 v13, 8, v13
	ds_bpermute_b32 v7, v7, v13
	s_waitcnt lgkmcnt(0)
	v_cndmask_b32_e32 v7, 0, v7, vcc
	v_add_u32_e32 v7, v7, v13
	ds_bpermute_b32 v8, v8, v7
	v_cmp_lt_i32_e32 vcc, v9, v6
	s_nop 1
	v_cndmask_b32_e32 v9, v9, v5, vcc
	v_cmp_lt_i32_e32 vcc, 1, v2
	v_lshlrev_b32_e32 v9, 2, v9
	s_waitcnt lgkmcnt(0)
	v_cndmask_b32_e32 v8, 0, v8, vcc
	v_add_u32_e32 v7, v8, v7
	ds_bpermute_b32 v8, v9, v7
	v_cmp_lt_i32_e32 vcc, v10, v6
	s_nop 1
	v_cndmask_b32_e32 v9, v10, v5, vcc
	v_cmp_lt_i32_e32 vcc, 3, v2
	v_lshlrev_b32_e32 v9, 2, v9
	s_waitcnt lgkmcnt(0)
	v_cndmask_b32_e32 v8, 0, v8, vcc
	v_add_u32_e32 v7, v8, v7
	ds_bpermute_b32 v8, v9, v7
	v_cmp_lt_i32_e32 vcc, v11, v6
	s_nop 1
	v_cndmask_b32_e32 v9, v11, v5, vcc
	v_cmp_lt_i32_e32 vcc, 7, v2
	v_lshlrev_b32_e32 v9, 2, v9
	s_waitcnt lgkmcnt(0)
	v_cndmask_b32_e32 v8, 0, v8, vcc
	v_add_u32_e32 v7, v8, v7
	ds_bpermute_b32 v8, v9, v7
	v_cmp_lt_i32_e32 vcc, v12, v6
	s_nop 1
	v_cndmask_b32_e32 v5, v12, v5, vcc
	v_cmp_lt_i32_e32 vcc, 15, v2
	v_lshlrev_b32_e32 v5, 2, v5
	s_waitcnt lgkmcnt(0)
	v_cndmask_b32_e32 v6, 0, v8, vcc
	v_add_u32_e32 v6, v6, v7
	ds_bpermute_b32 v5, v5, v6
	v_add_u32_e32 v7, 0x20100, v4
	v_cmp_lt_i32_e32 vcc, 31, v2
	ds_write_b32 v7, v3
	v_add_u32_e32 v4, 0x20200, v4
	s_waitcnt lgkmcnt(1)
	v_cndmask_b32_e32 v3, 0, v5, vcc
	v_add_u32_e32 v3, v3, v6
	v_sub_u32_e32 v5, v3, v13
	v_cmp_eq_u32_e32 vcc, 63, v2
	ds_write_b32 v4, v5
	s_and_b64 exec, exec, vcc
	s_add_i32 s5, 0, 0x20300
	v_mov_b32_e32 v2, s5
	ds_write_b32 v2, v3

; template <class P, class MK = NoChain>
; __device__ __forceinline__ void gemm_phase(LAS unsigned char* lds, const P& p, const MK& mk = MK(), bool chain_out = false, bool chained_in = false) {
;     ...
;     int tid = threadIdx.x; asm volatile("" : "+v"(tid));
;     const int wid = __builtin_amdgcn_readfirstlane(tid >> 6), lane = tid & 63, wr = wid >> 2, wc = wid & 3, fr = lane & 15, fq = lane >> 4;
;     unsigned voffB[2], vA[2][2], nvA[2][2], nvB[2]; typedef decltype(mk()) NP; constexpr int NES = NP::FP8 ? 1 : 2; constexpr int NBMODE = bmode_of<NP>::value; constexpr size_t nhstepB = (size_t)(NBMODE == 1 ? 8 : (NBMODE == 2 ? 16 : HALF)) * NP::LDB * NES;
;     constexpr size_t kstep = (size_t)(BK * 2);
;     constexpr int BMODE = bmode_of<P>::value;
;     constexpr size_t hstep = (size_t)(BMODE == 1 ? 8 : (BMODE == 2 ? 16 : HALF)) * LDB * ES, hstepA = (size_t)HALF * LDA * ES;
; #pragma unroll
;     for (int i = 0; i < 2; ++i) { int R, C; stage_rc(tid * 16 + i * 8192, R, C); const int rho_ = R & 31;
;         const int fq_ = (rho_ & 15) >> 2, n_ = rho_ >> 4, q_ = rho_ & 3;
;         const int Rb = BMODE == 1 ? ((R >> 5) * 64 + fq_ * 16 + 4 * n_ + q_) : (BMODE == 2 ? ((R >> 5) * 64 + 32 * (fq_ >> 1) + 8 * n_ + 4 * (fq_ & 1) + q_) : (P::PERM ? ((R & ~31) + perm32(R & 31)) : R));
;         voffB[i] = (unsigned)(Rb * LDB * ES + C * 2); vA[0][i] = (unsigned)(R * LDA * ES + C * 2); vA[1][i] = vA[0][i] + (unsigned)hstepA; nvA[0][i] = vA[0][i]; nvA[1][i] = vA[1][i]; nvB[i] = voffB[i]; }
;     const unsigned ldsw = (unsigned)wid * 1024u;
;     const int aoff = lds_byte(wr * 64 + fr, fq * 8), boff = lds_byte(wc * 32 + fr, fq * 8); const int aoff1 = aoff ^ 64, boff1 = boff ^ 64;
;     ...
;     Unit cur, nxt; int ui = 0;
;     if (!p.next(0, cur)) return;
;     Acc acc;
;     if constexpr (!PEEL) {
; #pragma unroll
;     for (int a = 0; a < 2; ++a)
; #pragma unroll
;         for (int b = 0; b < 2; ++b)
; #pragma unroll
;             for (int m = 0; m < 4; ++m)
; #pragma unroll
;                 for (int n = 0; n < 2; ++n) { typedef double d2_ __attribute__((ext_vector_type(2))); d2_ z_; asm volatile("v_mov_b64 %0, 0" : "=v"(z_.x)); asm volatile("v_mov_b64 %0, 0" : "=v"(z_.y)); acc[a][b][m][n] = __builtin_bit_cast(f32x4, z_); }
;     }
;     typedef int v8i_ __attribute__((ext_vector_type(8))); typedef int v4i_ __attribute__((ext_vector_type(4)));
.LBB0_2514:
	s_add_u32 s6, s2, 0x38400000
	s_addc_u32 s7, s3, 0
	s_add_u32 s42, s2, 0x2c000
	s_addc_u32 s43, s3, 0
	s_lshl_b32 s8, s8, 5
	s_and_b32 s10, s8, 0x60
	s_add_u32 s8, s20, 0x80
	s_addc_u32 s9, s21, 0
	s_add_i32 s44, s36, 0x18000
	s_mov_b32 m0, s44
	v_lshl_add_u64 v[4:5], s[8:9], 0, v[194:195]
	s_add_i32 s45, s36, 0x1a000
	global_load_lds_dwordx4 v[4:5], off
	v_lshl_add_u64 v[4:5], s[8:9], 0, v[196:197]
	s_add_u32 s8, s2, 0x36400080
	s_mov_b32 m0, s45
	s_addc_u32 s9, s3, 0
	s_add_i32 s46, s36, 0x8000
	global_load_lds_dwordx4 v[4:5], off
	s_mov_b32 m0, s46
	v_lshl_add_u64 v[4:5], s[8:9], 0, v[198:199]
	s_add_i32 s47, s36, 0xa000
	global_load_lds_dwordx4 v[4:5], off
	v_lshl_add_u64 v[4:5], s[8:9], 0, v[208:209]
	s_add_u32 s8, s20, 0x40080
	s_mov_b32 m0, s47
	s_addc_u32 s9, s21, 0
	s_add_i32 s48, s36, 0x1c000
	global_load_lds_dwordx4 v[4:5], off
	s_mov_b32 m0, s48
	v_lshl_add_u64 v[4:5], s[8:9], 0, v[194:195]
	s_add_i32 s49, s36, 0x1e000
	global_load_lds_dwordx4 v[4:5], off
	v_lshl_add_u64 v[4:5], s[8:9], 0, v[196:197]
	s_mov_b32 m0, s49
	v_lshrrev_b32_e32 v3, 4, v2
	global_load_lds_dwordx4 v[4:5], off
	v_and_b32_e32 v4, 15, v2
	v_bfe_u32 v5, v2, 4, 2
	v_bfe_u32 v2, v2, 1, 3
	v_lshl_or_b32 v1, s4, 6, v4
	v_bitop3_b32 v2, v3, v2, 3 bitop3:0x6c
	v_or_b32_e32 v4, s10, v4
	v_lshlrev_b32_e32 v6, 7, v1
	v_lshlrev_b32_e32 v2, 4, v2
	v_lshlrev_b32_e32 v4, 7, v4
	s_waitcnt vmcnt(10)
	s_barrier
	s_waitcnt vmcnt(6)
	v_or_b32_e32 v3, v6, v2
	v_or_b32_e32 v218, v4, v2
	v_bitop3_b32 v6, v6, 64, v2 bitop3:0x36
	v_bitop3_b32 v219, v4, 64, v2 bitop3:0x36
	v_lshlrev_b32_e32 v2, 2, v5
	s_add_u32 s8, s2, 0x36400100
	v_add_u32_e32 v220, 0x40000, v194
	v_add_u32_e32 v200, 0x40000, v196
	v_or_b32_e32 v221, s10, v2
	v_add_u32_e32 v222, 0x80, v1
	s_addc_u32 s9, s3, 0
	v_mov_b64_e32 v[202:203], 0x100
	v_mov_b64_e32 v[204:205], 0xff
	s_add_i32 s50, 0, 0x10000
	s_add_i32 s51, 0, 0x14000
	s_lshl_b32 s10, s10, 2
	v_lshlrev_b32_e32 v206, 2, v2
	s_mov_b32 s12, 0x3c800000
	v_add_u32_e32 v223, 0, v3
	v_add_u32_e32 v224, 0, v6
	v_mov_b32_e32 v214, v198
	v_mov_b32_e32 v198, v196
	v_mov_b32_e32 v225, v194
	s_mov_b32 s4, s5
	s_barrier
	s_branch .LBB0_2516

; #define LAS __attribute__((address_space(3)))
; __device__ __forceinline__ int otid() { int t = threadIdx.x; asm volatile("" : "+v"(t)); return t; }
; #define REP(k) for (int rep_ = 0; rep_ < ((REP_KIND == (k)) ? REP_N : 1); ++rep_)
; #define IN(k) (fresh_args()->ph_lo <= (k) && (k) < fresh_args()->ph_hi)
; #define PHASE_ARGS() CArgs* A_p = fresh_args(); CArgs& A = *A_p; unsigned char* ws = A.ws; (void)ws;
; __device__ __forceinline__ MoeTab moe_tables(CArgs& A, int l, LAS unsigned char* lds, bool want_order) {
;     MoeTab T; T.cnt = (LAS int*)(lds + LDS_TAB + 256); T.ts = T.cnt + 64; T.ord = (LAS int*)(lds + LDS_TAB + 1024) + 1;
;     unsigned* cg = (unsigned*)(A.ws + WS_CTL) + CW_CNT + l * 64;
;     const int tt = otid();
;     __syncthreads();
;     if (tt < 64) {
;         const int e = tt; const int c = (int)__hip_atomic_load(cg + e, RLX_AGENT);
;         T.cnt[e] = c;
;         const int nall = (c + 255) >> 8; const int ia = wave_incl_scan(nall, e);
;         T.ts[e] = ia - nall; if (e == 63) T.ts[64] = ia;
;         if (want_order) {
;             const int nfull = c >> 8, rem = c & 255;
;             const int n1 = nfull + (rem > 128 ? 1 : 0), nh = (rem != 0 && rem <= 128) ? 1 : 0;
;             const int p1 = wave_incl_scan(n1, e), ph = wave_incl_scan(nh, e);
;             const int tot1 = __builtin_amdgcn_readlane(p1, 63), toth = __builtin_amdgcn_readlane(ph, 63);
;             if (e < NT / 256) T.ord[e] = 64 | (e << 8);
;             const int pos = NT / 256 + p1 - n1;
; #pragma nounroll
;             for (int m = 0; m < n1; ++m) T.ord[pos + m] = e | (m << 8);
;             if (nh) T.ord[NT / 256 + tot1 + ph - 1] = e | (nfull << 8) | (1 << 16);
;             if (e == 0) T.ord[-1] = NT / 256 + tot1 + toth;
;         }
;     }
;     __syncthreads();
;     return T;
; }
; template <int l> __device__ __forceinline__ void layer_body(LAS unsigned char* lds, unsigned char* lds_raw, int bx, int vcu) {
;     ...
;         if (KEN(10) && IN(pb + 8)) REP(10) { PHASE_ARGS();
;             Moe2P P; P.ACT = (const char*)(ws + WS_ACT); P.SACT = (const char*)(ws + WS_SACT); P.W = (const char*)(ws + WS_W2E) + (size_t)l * NE * DM * DE; P.WS2 = (const char*)(ws + WS_W2S) + (size_t)l * DM * DS;
;             P.OUT2 = (bf16*)(ws + WS_OUT2); P.T = moe_tables(A, l, lds, true); P.G = G; P.c = bx;
.LBB0_2856:
	s_mov_b64 s[0:1], s[24:25]
	s_mov_b32 s0, s100
	s_waitcnt lgkmcnt(0)
	s_cmp_gt_i32 s0, 20
	s_cbranch_scc1 .LBB0_2932
	s_mov_b64 s[0:1], s[24:25]
	s_mov_b32 s0, s101
	s_waitcnt lgkmcnt(0)
	s_cmp_lt_i32 s0, 21
	s_cbranch_scc1 .LBB0_2932
	s_mov_b64 s[0:1], s[24:25]
	s_mov_b64 s[14:15], s[98:99]
	v_mov_b32_e32 v2, v0
	s_waitcnt vmcnt(0) lgkmcnt(0)
	s_mov_b64 vcc, 0
	s_barrier
	s_and_saveexec_b64 s[16:17], vcc
	s_cbranch_execz .LBB0_2877
	v_ashrrev_i32_e32 v3, 31, v2
	v_mul_u32_u24_e32 v4, 0x1100, v2
	v_mov_b32_e32 v5, 0
	v_lshl_add_u64 v[4:5], v[4:5], 0, s[14:15]
	v_add_co_u32_e32 v4, vcc, 0xc4000, v4
	v_cmp_lt_i32_e64 s[0:1], 0, v2
	s_nop 0
	v_addc_co_u32_e32 v5, vcc, 0, v5, vcc
	global_load_dword v3, v[4:5], off sc1
	v_mbcnt_lo_u32_b32 v4, -1, 0
	v_mbcnt_hi_u32_b32 v4, -1, v4
	v_and_b32_e32 v10, 64, v4
	v_add_u32_e32 v5, -1, v4
	v_cmp_lt_i32_e32 vcc, v5, v10
	v_add_u32_e32 v6, -2, v4
	v_add_u32_e32 v7, -4, v4
	v_cndmask_b32_e32 v5, v5, v4, vcc
	v_lshlrev_b32_e32 v5, 2, v5
	v_cmp_lt_i32_e32 vcc, v6, v10
	v_cmp_gt_i32_e64 s[2:3], 2, v2
	v_add_u32_e32 v8, -8, v4
	v_cndmask_b32_e32 v6, v6, v4, vcc
	v_lshlrev_b32_e32 v6, 2, v6
	v_cmp_lt_i32_e32 vcc, v7, v10
	v_cmp_gt_i32_e64 s[4:5], 4, v2
	v_add_u32_e32 v9, -16, v4
	v_cndmask_b32_e32 v7, v7, v4, vcc
	v_lshlrev_b32_e32 v7, 2, v7
	v_cmp_lt_i32_e32 vcc, v8, v10
	v_cmp_gt_i32_e64 s[6:7], 8, v2
	v_subrev_u32_e32 v11, 32, v4
	v_cndmask_b32_e32 v8, v8, v4, vcc
	v_lshlrev_b32_e32 v8, 2, v8
	v_cmp_lt_i32_e32 vcc, v9, v10
	v_cmp_gt_i32_e64 s[8:9], 16, v2
	v_cmp_gt_i32_e64 s[10:11], 32, v2
	v_cndmask_b32_e32 v9, v9, v4, vcc
	v_lshlrev_b32_e32 v9, 2, v9
	v_cmp_lt_i32_e32 vcc, v11, v10
	v_lshl_add_u32 v1, v2, 2, 0
	s_waitcnt vmcnt(0)
	v_add_u32_e32 v12, 0xff, v3
	v_ashrrev_i32_e32 v12, 8, v12
	ds_bpermute_b32 v13, v5, v12
	v_cndmask_b32_e32 v4, v11, v4, vcc
	v_lshlrev_b32_e32 v10, 2, v4
	v_cmp_eq_u32_e32 vcc, 63, v2
	s_waitcnt lgkmcnt(0)
	v_cndmask_b32_e64 v13, 0, v13, s[0:1]
	v_add_u32_e32 v13, v13, v12
	ds_bpermute_b32 v14, v6, v13
	s_waitcnt lgkmcnt(0)
	v_cndmask_b32_e64 v14, v14, 0, s[2:3]
	v_add_u32_e32 v13, v14, v13
	ds_bpermute_b32 v14, v7, v13
	s_waitcnt lgkmcnt(0)
	v_cndmask_b32_e64 v14, v14, 0, s[4:5]
	v_add_u32_e32 v13, v14, v13
	ds_bpermute_b32 v14, v8, v13
	s_waitcnt lgkmcnt(0)
	v_cndmask_b32_e64 v14, v14, 0, s[6:7]
	v_add_u32_e32 v13, v14, v13
	ds_bpermute_b32 v14, v9, v13
	s_waitcnt lgkmcnt(0)
	v_cndmask_b32_e64 v4, v14, 0, s[8:9]
	v_add_u32_e32 v4, v4, v13
	ds_bpermute_b32 v11, v10, v4
	v_add_u32_e32 v13, 0x20100, v1
	v_add_u32_e32 v14, 0x20200, v1
	ds_write_b32 v13, v3
	s_waitcnt lgkmcnt(1)
	v_cndmask_b32_e64 v11, v11, 0, s[10:11]
	v_add_u32_e32 v4, v11, v4
	v_sub_u32_e32 v11, v4, v12
	ds_write_b32 v14, v11
	s_and_saveexec_b64 s[12:13], vcc
	s_add_i32 s18, 0, 0x20300
	v_mov_b32_e32 v11, s18
	ds_write_b32 v11, v4
	s_or_b64 exec, exec, s[12:13]
	s_movk_i32 s18, 0x80
	v_ashrrev_i32_e32 v12, 8, v3
	v_cmp_gt_u32_sdwa s[12:13], v3, s18 src0_sel:BYTE_0 src1_sel:DWORD
	v_mov_b32_e32 v11, -1
	v_add_u32_sdwa v11, v3, v11 dst_sel:DWORD dst_unused:UNUSED_PAD src0_sel:BYTE_0 src1_sel:DWORD
	v_addc_co_u32_e64 v4, vcc, 0, v12, s[12:13]
	v_cmp_gt_u32_e32 vcc, s18, v11
	ds_bpermute_b32 v13, v5, v4
	s_nop 0
	v_cndmask_b32_e64 v11, 0, 1, vcc
	ds_bpermute_b32 v5, v5, v11
	s_waitcnt lgkmcnt(1)
	v_cndmask_b32_e64 v11, 0, v13, s[0:1]
	v_addc_co_u32_e64 v12, s[12:13], v11, v12, s[12:13]
	s_waitcnt lgkmcnt(0)
	v_cndmask_b32_e64 v5, 0, v5, s[0:1]
	v_addc_co_u32_e64 v14, s[0:1], 0, v5, vcc
	ds_bpermute_b32 v13, v6, v12
	ds_bpermute_b32 v14, v6, v14
	s_waitcnt lgkmcnt(1)
	v_cndmask_b32_e64 v6, v13, 0, s[2:3]
	s_waitcnt lgkmcnt(0)
	v_cndmask_b32_e64 v14, v14, 0, s[2:3]
	v_add_u32_e32 v12, v6, v12
	v_addc_co_u32_e64 v5, s[0:1], v14, v5, vcc
	ds_bpermute_b32 v13, v7, v12
	ds_bpermute_b32 v14, v7, v5
	s_waitcnt lgkmcnt(1)
	v_cndmask_b32_e64 v7, v13, 0, s[4:5]
	s_waitcnt lgkmcnt(0)
	v_cndmask_b32_e64 v14, v14, 0, s[4:5]
	v_add_u32_e32 v13, v7, v12
	v_add_u32_e32 v5, v14, v5
	ds_bpermute_b32 v12, v8, v13
	ds_bpermute_b32 v8, v8, v5
	s_waitcnt lgkmcnt(1)
	v_cndmask_b32_e64 v12, v12, 0, s[6:7]
	s_waitcnt lgkmcnt(0)
	v_cndmask_b32_e64 v8, v8, 0, s[6:7]
	v_add_u32_e32 v13, v12, v13
	v_add_u32_e32 v5, v8, v5
	ds_bpermute_b32 v14, v9, v13
	ds_bpermute_b32 v8, v9, v5
	s_waitcnt lgkmcnt(1)
	v_cndmask_b32_e64 v9, v14, 0, s[8:9]
	s_waitcnt lgkmcnt(0)
	v_cndmask_b32_e64 v8, v8, 0, s[8:9]
	v_add_u32_e32 v13, v9, v13
	v_add_u32_e32 v5, v8, v5
	ds_bpermute_b32 v14, v10, v13
	ds_bpermute_b32 v10, v10, v5
	s_waitcnt lgkmcnt(1)
	v_cndmask_b32_e64 v8, v14, 0, s[10:11]
	s_waitcnt lgkmcnt(0)
	v_cndmask_b32_e64 v10, v10, 0, s[10:11]
	v_add_u32_e32 v13, v8, v13
	v_add_u32_e32 v5, v10, v5
	v_readlane_b32 s8, v13, 63
	v_readlane_b32 s9, v5, 63
	s_and_saveexec_b64 s[0:1], s[10:11]
	v_add_u32_e32 v1, 0x20404, v1
	v_lshl_or_b32 v10, v2, 8, 64
	ds_write_b32 v1, v10
	s_or_b64 exec, exec, s[0:1]
	v_cmp_lt_i32_e64 s[0:1], 0, v4
	s_and_saveexec_b64 s[2:3], s[0:1]
	s_cbranch_execz .LBB0_2873
	v_add3_u32 v1, v11, v6, v7
	s_mov_b32 s10, 1
	v_cmp_ne_u32_e64 s[0:1], 1, v4
	s_mov_b64 s[6:7], 0
	v_add3_u32 v9, v1, v12, v9
	s_and_saveexec_b64 s[4:5], s[0:1]
	s_xor_b64 s[4:5], exec, s[4:5]
	s_cbranch_execnz .LBB0_2867
	s_andn2_saveexec_b64 s[0:1], s[4:5]
	s_cbranch_execnz .LBB0_2870

; #define LAS __attribute__((address_space(3)))
; __device__ __forceinline__ int otid() { int t = threadIdx.x; asm volatile("" : "+v"(t)); return t; }
; __device__ __forceinline__ MoeTab moe_tables(CArgs& A, int l, LAS unsigned char* lds, bool want_order) {
;     MoeTab T; T.cnt = (LAS int*)(lds + LDS_TAB + 256); T.ts = T.cnt + 64; T.ord = (LAS int*)(lds + LDS_TAB + 1024) + 1;
;     unsigned* cg = (unsigned*)(A.ws + WS_CTL) + CW_CNT + l * 64;
;     const int tt = otid();
;     __syncthreads();
;     if (tt < 64) {
;         const int e = tt; const int c = (int)__hip_atomic_load(cg + e, RLX_AGENT);
;         T.cnt[e] = c;
;         const int nall = (c + 255) >> 8; const int ia = wave_incl_scan(nall, e);
;         T.ts[e] = ia - nall; if (e == 63) T.ts[64] = ia;
; __device__ __forceinline__ void combine_phase(CArgs& A, int l, const float* xin, LAS unsigned char* lds, int vcu, int G) {
;     int tid = threadIdx.x; asm volatile("" : "+v"(tid));
;     const int lane = tid & 63, wave = __builtin_amdgcn_readfirstlane(tid >> 6);
;     const MoeTab T = moe_tables(A, l, lds, false);
.LBB0_2990:
	s_mov_b64 s[0:1], s[24:25]
	s_mov_b32 s0, s100
	s_waitcnt lgkmcnt(0)
	s_cmp_gt_i32 s0, 21
	s_cbranch_scc1 .LBB0_2999
	s_mov_b64 s[0:1], s[24:25]
	s_mov_b32 s0, s101
	s_waitcnt lgkmcnt(0)
	s_cmp_lt_i32 s0, 22
	s_cbranch_scc1 .LBB0_2999
	s_mov_b64 s[10:11], s[24:25]
	s_mov_b64 s[4:5], s[98:99]
	v_mov_b32_e32 v1, v0
	v_mov_b32_e32 v2, v0
	s_waitcnt vmcnt(0) lgkmcnt(0)
	v_readfirstlane_b32 s2, v1
	s_mov_b64 vcc, 0
	s_barrier
	s_and_saveexec_b64 s[0:1], vcc
	s_cbranch_execz .LBB0_2995
	v_ashrrev_i32_e32 v3, 31, v2
	v_mul_u32_u24_e32 v4, 0x1100, v2
	v_mov_b32_e32 v5, 0
	v_lshl_add_u64 v[4:5], v[4:5], 0, s[4:5]
	v_add_co_u32_e32 v4, vcc, 0xc4000, v4
	s_nop 1
	v_addc_co_u32_e32 v5, vcc, 0, v5, vcc
	global_load_dword v3, v[4:5], off sc1
	v_mbcnt_lo_u32_b32 v5, -1, 0
	v_mbcnt_hi_u32_b32 v5, -1, v5
	v_and_b32_e32 v6, 64, v5
	v_add_u32_e32 v7, -1, v5
	v_cmp_lt_i32_e32 vcc, v7, v6
	v_add_u32_e32 v8, -2, v5
	v_add_u32_e32 v9, -4, v5
	v_cndmask_b32_e32 v7, v7, v5, vcc
	v_lshlrev_b32_e32 v7, 2, v7
	v_cmp_lt_i32_e32 vcc, v8, v6
	v_add_u32_e32 v10, -8, v5
	v_add_u32_e32 v11, -16, v5
	v_cndmask_b32_e32 v8, v8, v5, vcc
	v_cmp_lt_i32_e32 vcc, 0, v2
	v_lshlrev_b32_e32 v8, 2, v8
	v_subrev_u32_e32 v12, 32, v5
	v_lshl_add_u32 v4, v2, 2, 0
	s_waitcnt vmcnt(0)
	v_add_u32_e32 v13, 0xff, v3
	v_ashrrev_i32_e32 v13, 8, v13
	ds_bpermute_b32 v7, v7, v13
	s_waitcnt lgkmcnt(0)
	v_cndmask_b32_e32 v7, 0, v7, vcc
	v_add_u32_e32 v7, v7, v13
	ds_bpermute_b32 v8, v8, v7
	v_cmp_lt_i32_e32 vcc, v9, v6
	s_nop 1
	v_cndmask_b32_e32 v9, v9, v5, vcc
	v_cmp_lt_i32_e32 vcc, 1, v2
	v_lshlrev_b32_e32 v9, 2, v9
	s_waitcnt lgkmcnt(0)
	v_cndmask_b32_e32 v8, 0, v8, vcc
	v_add_u32_e32 v7, v8, v7
	ds_bpermute_b32 v8, v9, v7
	v_cmp_lt_i32_e32 vcc, v10, v6
	s_nop 1
	v_cndmask_b32_e32 v9, v10, v5, vcc
	v_cmp_lt_i32_e32 vcc, 3, v2
	v_lshlrev_b32_e32 v9, 2, v9
	s_waitcnt lgkmcnt(0)
	v_cndmask_b32_e32 v8, 0, v8, vcc
	v_add_u32_e32 v7, v8, v7
	ds_bpermute_b32 v8, v9, v7
	v_cmp_lt_i32_e32 vcc, v11, v6
	s_nop 1
	v_cndmask_b32_e32 v9, v11, v5, vcc
	v_cmp_lt_i32_e32 vcc, 7, v2
	v_lshlrev_b32_e32 v9, 2, v9
	s_waitcnt lgkmcnt(0)
	v_cndmask_b32_e32 v8, 0, v8, vcc
	v_add_u32_e32 v7, v8, v7
	ds_bpermute_b32 v8, v9, v7
	v_cmp_lt_i32_e32 vcc, v12, v6
	s_nop 1
	v_cndmask_b32_e32 v5, v12, v5, vcc
	v_cmp_lt_i32_e32 vcc, 15, v2
	v_lshlrev_b32_e32 v5, 2, v5
	s_waitcnt lgkmcnt(0)
	v_cndmask_b32_e32 v6, 0, v8, vcc
	v_add_u32_e32 v6, v6, v7
	ds_bpermute_b32 v5, v5, v6
	v_add_u32_e32 v7, 0x20100, v4
	v_cmp_lt_i32_e32 vcc, 31, v2
	ds_write_b32 v7, v3
	v_add_u32_e32 v4, 0x20200, v4
	s_waitcnt lgkmcnt(1)
	v_cndmask_b32_e32 v3, 0, v5, vcc
	v_add_u32_e32 v3, v3, v6
	v_sub_u32_e32 v5, v3, v13
	v_cmp_eq_u32_e32 vcc, 63, v2
	ds_write_b32 v4, v5
	s_and_b64 exec, exec, vcc
	s_add_i32 s3, 0, 0x20300
	v_mov_b32_e32 v2, s3
	ds_write_b32 v2, v3
